# second WG per CU also staggered (1792 cycles) at the start of the xBC-conv, SSD-output/S5-GEMM and GLU/gate phases
# speedup vs baseline: 1.0452x; 1.0029x over previous
; #define LAS __attribute__((address_space(3)))
; #define PR_BEGIN(id) do { if (PROBE_SP == (id)) c.prt = __builtin_amdgcn_s_memrealtime(); } while (0)
; #define PR_END(id) do { if (PROBE_SP == (id)) c.pracc += __builtin_amdgcn_s_memrealtime() - c.prt; } while (0)
;     template <class T> __device__ __forceinline__ T* w(size_t off) const { return (T*)(p->ws + off); }
; __device__ __forceinline__ void ph_norm1(const Ctx& c, int layer, int gw, int nwaves, unsigned char* lds) {
;     const int lane = c.tid & 63;
;     bf16* HA = c.w<bf16>(WS_HA); float* DTR = c.w<float>(WS_DTR);
;     const float* MOD = c.w<float>(WS_MOD) + (size_t)layer * 5 * 6144;
;     const float* g = c.in(6) + layer * D;
;     __syncthreads();
;     {
;         f32x4 w8[8];
; #pragma unroll
;         for (int j = 0; j < 8; ++j) w8[j] = ((const f32x4*)(c.w<float>(WS_WDT) + (size_t)layer * 8 * 1024))[c.tid + NTHR * j];
; #pragma unroll
;         for (int j = 0; j < 8; ++j) ((LAS f32x4*)lds)[c.tid + NTHR * j] = w8[j];
;     }
;     __syncthreads();
;     const LAS float* wdt = (const LAS float*)lds;
;     f32x4 gv[4];
; #pragma unroll
;     for (int i = 0; i < 4; ++i) gv[i] = *(const f32x4*)(g + (lane + 64 * i) * 4);
; __global__ void __launch_bounds__(NTHR, 2) mk_fwd(Params prm) {
;     ...
;     for (int ph = prm.ph_lo; ph < prm.ph_hi; ++ph) {
;         if (PROBE_SP >= 0) pr_t0 = __builtin_amdgcn_s_memrealtime();
;         asm volatile("" : "+s"(c.p));
;         { int t_ = threadIdx.x; asm volatile("" : "+v"(t_)); c.tid = t_; }
;         if (ph == 0) {
;             const bool split = G >= 384;
;             const int g2 = split ? (bid >= 256 ? gtid - 65536 : 0x3fffffff) : gtid, gth2 = split ? gthreads - 65536 : gthreads;
;             ph_prep(c, g2, gth2, bid, G, (float*)smem_raw); PR_BEGIN(124); cvt_small(c, g2, gth2); PR_END(124); }
;         else if (ph == 1) ph_norm1(c, 0, gw, nwaves, smem_raw);
.LBB0_13:
	ds_read_b32 v2, v146
	s_waitcnt lgkmcnt(0)
	v_readfirstlane_b32 s7, v2
	s_cmp_eq_u32 s7, 0
	s_cbranch_scc1 .Lstag_done
	s_lshr_b32 s6, 0x10884, s66
	s_bitcmp1_b32 s6, 0
	s_cbranch_scc0 .Lstag_n0
	s_sleep 14
.Lstag_n0:
	s_lshr_b32 s6, 0xd068, s66
	s_bitcmp1_b32 s6, 0
	s_cbranch_scc0 .Lstag_n1
	s_sleep 28
.Lstag_n1:
.Lstag_done:
	s_mov_b64 s[4:5], s[0:1]
	v_mov_b32_e32 v156, v0
	s_mov_b64 s[6:7], -1
	s_mov_b64 s[28:29], 0
	s_cmp_lt_i32 s66, 1
	s_mov_b64 s[0:1], 0
	s_cbranch_scc1 .LBB0_22
	s_cmp_eq_u32 s66, 1
	s_mov_b64 s[0:1], -1
	s_cbranch_scc0 .LBB0_26
	s_load_dwordx2 s[0:1], s[4:5], 0x130
	v_ashrrev_i32_e32 v157, 31, v156
	s_waitcnt lgkmcnt(0)
	s_barrier
	v_lshl_add_u64 v[20:21], v[156:157], 4, s[0:1]
	s_waitcnt vmcnt(0)
	v_add_co_u32_e32 v4, vcc, 0x1803d000, v20
	v_readlane_b32 s6, v253, 6
	s_nop 0
	v_addc_co_u32_e32 v5, vcc, 0, v21, vcc
	v_add_co_u32_e32 v8, vcc, 0x1803e000, v20
	v_add_u32_e32 v2, s6, v156
	s_nop 0
	v_addc_co_u32_e32 v9, vcc, 0, v21, vcc
	v_add_co_u32_e32 v12, vcc, 0x1803f000, v20
	global_load_dwordx4 v[4:7], v[4:5], off offset:256
	s_nop 0
	global_load_dwordx4 v[8:11], v[8:9], off offset:256
	v_addc_co_u32_e32 v13, vcc, 0, v21, vcc
	v_add_co_u32_e32 v16, vcc, 0x18040000, v20
	s_movk_i32 s6, 0x4400
	s_nop 0
	v_addc_co_u32_e32 v17, vcc, 0, v21, vcc
	v_add_co_u32_e32 v22, vcc, 0x18041000, v20
	global_load_dwordx4 v[12:15], v[12:13], off offset:256
	s_nop 0
	global_load_dwordx4 v[16:19], v[16:17], off offset:256
	v_addc_co_u32_e32 v23, vcc, 0, v21, vcc
	v_add_co_u32_e32 v26, vcc, 0x18042000, v20
	s_nop 1
	v_addc_co_u32_e32 v27, vcc, 0, v21, vcc
	v_add_co_u32_e32 v30, vcc, 0x18043000, v20
	global_load_dwordx4 v[22:25], v[22:23], off offset:256
	s_nop 0
	global_load_dwordx4 v[26:29], v[26:27], off offset:256
	v_addc_co_u32_e32 v31, vcc, 0, v21, vcc
	v_add_co_u32_e32 v20, vcc, 0x18044000, v20
	s_nop 1
	v_addc_co_u32_e32 v21, vcc, 0, v21, vcc
	global_load_dwordx4 v[30:33], v[30:31], off offset:256
	s_nop 0
	global_load_dwordx4 v[34:37], v[20:21], off offset:256
	v_ashrrev_i32_e32 v20, 6, v2
	v_lshlrev_b32_e32 v21, 4, v156
	v_cmp_gt_i32_e32 vcc, s6, v20
	s_waitcnt vmcnt(7)
	ds_write_b128 v21, v[4:7]
	s_waitcnt vmcnt(6)
	ds_write_b128 v21, v[8:11] offset:4096
	s_waitcnt vmcnt(5)
	ds_write_b128 v21, v[12:15] offset:8192
	s_waitcnt vmcnt(4)
	ds_write_b128 v21, v[16:19] offset:12288
	s_waitcnt vmcnt(3)
	ds_write_b128 v21, v[22:25] offset:16384
	s_waitcnt vmcnt(2)
	ds_write_b128 v21, v[26:29] offset:20480
	s_waitcnt vmcnt(1)
	ds_write_b128 v21, v[30:33] offset:24576
	s_waitcnt vmcnt(0)
	ds_write_b128 v21, v[34:37] offset:28672
	s_waitcnt lgkmcnt(0)
	s_barrier
	s_and_saveexec_b64 s[42:43], vcc
	s_cbranch_execz .LBB0_25
	s_load_dwordx2 s[6:7], s[4:5], 0x30
	v_and_b32_e32 v50, 63, v156
	v_lshlrev_b32_e32 v51, 4, v50
	v_cmp_lt_i32_e32 vcc, v229, v228
	s_add_u32 s44, s0, 0x100000
	s_waitcnt lgkmcnt(0)
	global_load_dwordx4 v[4:7], v51, s[6:7]
	global_load_dwordx4 v[8:11], v51, s[6:7] offset:1024
	global_load_dwordx4 v[12:15], v51, s[6:7] offset:2048
	global_load_dwordx4 v[16:19], v51, s[6:7] offset:3072
	v_cndmask_b32_e32 v21, v222, v229, vcc
	v_cmp_lt_i32_e32 vcc, v230, v228
	v_lshlrev_b32_e32 v52, 2, v21
	v_lshlrev_b32_e32 v2, 2, v50
	v_cndmask_b32_e32 v21, v222, v230, vcc
	v_cmp_lt_i32_e32 vcc, v231, v228
	v_lshlrev_b32_e32 v53, 2, v21
	v_lshlrev_b32_e32 v24, 3, v50
	v_cndmask_b32_e32 v21, v222, v231, vcc
	v_cmp_lt_i32_e32 vcc, v232, v228
	v_lshlrev_b32_e32 v54, 2, v21
	v_mov_b32_e32 v25, v3
	v_cndmask_b32_e32 v21, v222, v232, vcc
	v_cmp_lt_i32_e32 vcc, v233, v228
	v_lshlrev_b32_e32 v55, 2, v21
	s_addc_u32 s45, s1, 0
	v_cndmask_b32_e32 v21, v222, v233, vcc
	v_cmp_lt_i32_e32 vcc, v234, v228
	v_or_b32_e32 v28, 0x100, v2
	v_or_b32_e32 v30, 0x200, v2
	v_or_b32_e32 v32, 0x300, v2
	v_lshlrev_b32_e32 v56, 2, v21
	v_cndmask_b32_e32 v21, v222, v234, vcc
	v_lshl_add_u64 v[22:23], s[0:1], 0, v[2:3]
	s_mov_b64 s[6:7], 0x1034c000
	v_lshl_add_u64 v[24:25], s[0:1], 0, v[24:25]
	s_mov_b64 s[0:1], 0x45c6000
	v_lshlrev_b32_e32 v57, 2, v21
	v_cmp_gt_u32_e32 vcc, 8, v50
	v_lshl_add_u64 v[22:23], v[22:23], 0, s[6:7]
	v_lshl_add_u64 v[24:25], v[24:25], 0, s[0:1]
	s_mov_b64 s[46:47], 0
	v_lshlrev_b32_e32 v26, 2, v2
	v_lshlrev_b32_e32 v28, 2, v28
	v_lshlrev_b32_e32 v30, 2, v30
	v_lshlrev_b32_e32 v32, 2, v32
	v_mov_b32_e32 v27, v3
	v_mov_b32_e32 v29, v3
	v_mov_b32_e32 v31, v3
	v_mov_b32_e32 v33, v3
	s_branch .LBB0_18
